# v022-prio-by-remaining-tiles-plus-clamp-removal
# speedup vs baseline: 1.0810x; 1.0158x over previous
.LBB3_8:
	s_or_b64 exec, exec, s[2:3]
	s_movk_i32 s15, 0x61a8
	v_cmp_gt_i32_e32 vcc, s15, v56
	s_waitcnt lgkmcnt(0)
	s_barrier
	s_and_saveexec_b64 s[2:3], vcc
	s_cbranch_execz .LBB3_73
	s_load_dwordx4 s[16:19], s[0:1], 0x30
	v_and_b32_e32 v1, 63, v0
	s_waitcnt vmcnt(3)
	v_mov_b32_e32 v2, 0x3e020821
	v_cmp_gt_u32_e64 s[0:1], 32, v1
	v_mov_b32_e32 v65, 0xffff
	v_cmp_ne_u32_e32 vcc, 0, v52
	v_cndmask_b32_e64 v64, v2, 0, s[0:1]
	s_waitcnt vmcnt(0)
	v_lshrrev_b32_e32 v2, 16, v53
	v_lshrrev_b32_e32 v0, 1, v0
	v_mov_b32_e32 v3, 0x7a00
	v_ashrrev_i32_e32 v57, 31, v56
	v_cndmask_b32_e32 v77, v65, v2, vcc
	s_lshl_b32 s6, s6, 2
	v_lshlrev_b32_e32 v2, 4, v1
	v_and_or_b32 v67, v0, 16, v3
	v_lshlrev_b32_e32 v70, 1, v1
	v_lshlrev_b32_e32 v36, 2, v1
	v_lshlrev_b64 v[0:1], 8, v[56:57]
	v_mov_b32_e32 v37, 0
	v_or_b32_e32 v0, v0, v36
	s_ashr_i32 s7, s6, 31
	s_mov_b32 s5, 0
	v_add_u32_e32 v66, 0x3200, v2
	v_add_u32_e32 v68, 0x5200, v2
	v_add_u32_e32 v69, 0x7200, v2
	s_waitcnt lgkmcnt(0)
	v_lshl_add_u64 v[58:59], s[16:17], 0, v[36:37]
	v_lshl_add_u64 v[60:61], s[18:19], 0, v[0:1]
	s_lshl_b64 s[10:11], s[6:7], 8
	s_mov_b64 s[12:13], 0
	s_movk_i32 s7, 0x61a7
	v_mov_b32_e32 v57, 0xc0669d92
	s_mov_b32 s20, 0xc1c00000
	v_mov_b32_e32 v71, 0x41c00000
	v_mov_b32_e32 v72, 0xbfb8aa3b
	v_mov_b32_e32 v73, 0xc1b69213
	v_mov_b32_e32 v74, 0xc228283a
	v_mov_b32_e32 v75, 0xc275076b
	s_mov_b32 s14, 0x3e0a9555
	v_readfirstlane_b32 s94, v56
	s_nop 3
	s_branch .LBB3_11

.LBB3_11:
	s_sub_u32 s95, 0x61a7, s94
	s_lshr_b32 s95, s95, 12
	s_cmp_ge_u32 s95, 3
	s_cbranch_scc1 .Lprio_e0_3
	s_cmp_ge_u32 s95, 2
	s_cbranch_scc1 .Lprio_e0_2
	s_cmp_ge_u32 s95, 1
	s_cbranch_scc1 .Lprio_e0_1
	s_setprio 0
	s_branch .Lprio_e0_done

.Lprio_e0_done:
	s_add_u32 s94, s94, 0x1000
	v_sub_f32_e32 v36, v32, v64
	v_fmamk_f32 v38, v36, 0x4297576a, v57
	v_fmamk_f32 v39, v36, 0x4297576a, v73
	v_med3_f32 v41, v38, s20, v71
	v_med3_f32 v43, v39, s20, v71
	v_mul_f32_e64 v38, v41, -v41
	v_mul_f32_e64 v39, v43, -v43
	v_exp_f32_e32 v38, v38
	v_exp_f32_e32 v39, v39
	v_fmamk_f32 v40, v41, 0x4019be61, v72
	v_fmamk_f32 v41, v41, 0xc019be61, v72
	v_exp_f32_e32 v42, v41
	v_pk_mul_f32 v[46:47], v[32:33], v[38:39] op_sel:[1,0]
	v_fmamk_f32 v38, v43, 0x4019be61, v72
	v_exp_f32_e32 v41, v38
	v_fmamk_f32 v38, v43, 0xc019be61, v72
	v_exp_f32_e32 v43, v38
	v_fmamk_f32 v38, v36, 0x4297576a, v74
	v_fmamk_f32 v36, v36, 0x4297576a, v75
	v_med3_f32 v45, v38, s20, v71
	v_med3_f32 v36, v36, s20, v71
	v_mul_f32_e64 v38, v45, -v45
	v_mul_f32_e64 v39, v36, -v36
	v_exp_f32_e32 v38, v38
	v_exp_f32_e32 v39, v39
	v_exp_f32_e32 v40, v40
	v_fmamk_f32 v44, v45, 0x4019be61, v72
	v_fmamk_f32 v45, v45, 0xc019be61, v72
	v_pk_mul_f32 v[54:55], v[32:33], v[38:39] op_sel:[1,0]
	v_fmamk_f32 v38, v36, 0x4019be61, v72
	v_exp_f32_e32 v48, v45
	v_exp_f32_e32 v45, v38
	v_pk_mul_f32 v[50:51], v[40:41], v[46:47]
	v_pk_mul_f32 v[38:39], v[40:41], s[14:15] op_sel_hi:[1,0]
	v_exp_f32_e32 v44, v44
	v_pk_mul_f32 v[52:53], v[38:39], v[50:51]
	v_pk_mul_f32 v[38:39], v[38:39], s[14:15] op_sel_hi:[1,0]
	ds_read_b128 v[12:15], v66
	ds_read_b128 v[8:11], v66 offset:1024
	ds_read_b128 v[4:7], v66 offset:2048
	ds_read_b128 v[0:3], v66 offset:3072
	ds_read_b128 v[16:19], v67
	ds_read_b128 v[20:23], v67 offset:32
	ds_read_b128 v[24:27], v67 offset:64
	ds_read_b128 v[28:31], v67 offset:96
	v_pk_mul_f32 v[78:79], v[38:39], v[52:53]
	v_pk_mul_f32 v[38:39], v[38:39], s[14:15] op_sel_hi:[1,0]
	v_pk_mul_f32 v[82:83], v[42:43], v[46:47]
	v_pk_mul_f32 v[80:81], v[38:39], v[78:79]
	v_pk_mul_f32 v[38:39], v[42:43], s[14:15] op_sel_hi:[1,0]
	v_pk_mul_f32 v[86:87], v[44:45], v[54:55]
	v_pk_mul_f32 v[42:43], v[38:39], v[82:83]
	v_pk_mul_f32 v[38:39], v[38:39], s[14:15] op_sel_hi:[1,0]
	v_cvt_pk_f16_f32 v40, v50, v52
	v_pk_mul_f32 v[84:85], v[38:39], v[42:43]
	v_pk_mul_f32 v[38:39], v[44:45], s[14:15] op_sel_hi:[1,0]
	v_cvt_pk_f16_f32 v41, v78, v80
	v_pk_mul_f32 v[88:89], v[38:39], v[86:87]
	v_pk_mul_f32 v[38:39], v[38:39], s[14:15] op_sel_hi:[1,0]
	v_fmamk_f32 v36, v36, 0xc019be61, v72
	v_pk_mul_f32 v[90:91], v[38:39], v[88:89]
	v_pk_mul_f32 v[44:45], v[38:39], s[14:15] op_sel_hi:[1,0]
	v_cvt_pk_f16_f32 v38, v84, v42
	v_cvt_pk_f16_f32 v39, v82, v46
	v_cvt_pk_f16_f32 v42, v85, v43
	v_cvt_pk_f16_f32 v43, v83, v47
	s_waitcnt lgkmcnt(0)
	v_mfma_f32_32x32x16_f16 v[16:31], v[12:15], v[38:41], v[16:31]
	v_mul_f32_e64 v12, v44, v90
	v_mul_f32_e64 v13, v45, v91
	v_cvt_pk_f16_f32 v44, v51, v53
	v_cvt_pk_f16_f32 v45, v79, v81
	v_exp_f32_e32 v49, v36
	ds_read_b128 v[50:53], v66 offset:4096
	v_cvt_pk_f16_f32 v82, v87, v89
	v_cvt_pk_f16_f32 v83, v91, v13
	v_mfma_f32_32x32x16_f16 v[16:31], v[8:11], v[42:45], v[16:31]
	v_mul_f32_e64 v14, v48, v54
	v_mul_f32_e64 v15, v49, v55
	v_mul_f32_e64 v48, v48, s14
	v_mul_f32_e64 v49, v49, s14
	v_cvt_pk_f16_f32 v47, v14, v54
	v_pk_mul_f32 v[8:9], v[48:49], v[14:15]
	v_pk_mul_f32 v[10:11], v[48:49], s[14:15] op_sel_hi:[1,0]
	v_cvt_pk_f16_f32 v48, v86, v88
	v_pk_mul_f32 v[10:11], v[10:11], v[8:9]
	v_cvt_pk_f16_f32 v49, v90, v12
	v_cvt_pk_f16_f32 v46, v10, v8
	v_cvt_pk_f16_f32 v80, v11, v9
	v_cvt_pk_f16_f32 v81, v15, v55
	v_mfma_f32_32x32x16_f16 v[16:31], v[4:7], v[46:49], v[16:31]
	v_mov_b32_e32 v36, v56
	v_add_u32_e32 v56, s6, v36
	v_cmp_gt_i32_e32 vcc, s15, v56
	v_mov_b32_e32 v78, v63
	v_readlane_b32 s21, v35, 0
	v_cndmask_b32_e32 v36, v36, v56, vcc
	v_cmp_ne_u32_sdwa s[16:17], v78, v34 src0_sel:WORD_1 src1_sel:WORD_1
	v_mfma_f32_32x32x16_f16 v[16:31], v[0:3], v[80:83], v[16:31]
	ds_read_b128 v[0:3], v67 offset:128
	ds_read_b128 v[4:7], v67 offset:160
	ds_read_b128 v[8:11], v67 offset:192
	ds_read_b128 v[12:15], v67 offset:224
	ds_read_b128 v[84:87], v66 offset:5120
	s_nop 0
	s_nop 0
	s_nop 0
	s_nop 0
	s_nop 0
	s_nop 0
	s_waitcnt lgkmcnt(1)
	v_mfma_f32_32x32x16_f16 v[0:15], v[50:53], v[38:41], v[0:15]
	ds_read_b128 v[38:41], v66 offset:6144
	ds_read_b128 v[50:53], v66 offset:7168
	s_nop 0
	s_nop 0
	s_nop 2
	v_exp_f32_e32 v16, v16
	v_exp_f32_e32 v17, v17
	v_exp_f32_e32 v18, v18
	s_waitcnt lgkmcnt(2)
	v_mfma_f32_32x32x16_f16 v[0:15], v[84:87], v[42:45], v[0:15]
	v_exp_f32_e32 v19, v19
	v_exp_f32_e32 v20, v20
	v_exp_f32_e32 v21, v21
	v_exp_f32_e32 v22, v22
	v_exp_f32_e32 v23, v23
	v_pk_add_f32 v[16:17], v[16:17], 1.0 op_sel_hi:[1,0]
	v_pk_add_f32 v[18:19], v[18:19], 1.0 op_sel_hi:[1,0]
	s_waitcnt lgkmcnt(1)
	v_mfma_f32_32x32x16_f16 v[0:15], v[38:41], v[46:49], v[0:15]
	v_add_f32_e64 v20, v20, 1.0
	v_add_f32_e64 v21, v21, 1.0
	v_add_f32_e64 v22, v22, 1.0
	v_add_f32_e64 v23, v23, 1.0
	v_log_f32_e32 v16, v16
	v_log_f32_e32 v17, v17
	v_log_f32_e32 v18, v18
	v_log_f32_e32 v19, v19
	v_log_f32_e32 v20, v20
	s_waitcnt lgkmcnt(0)
	v_mfma_f32_32x32x16_f16 v[0:15], v[50:53], v[80:83], v[0:15]
	s_nop 0
	s_nop 0
	s_nop 0
	s_nop 0
	s_nop 0
	s_nop 0
	s_nop 11
	v_exp_f32_e32 v6, v6
	v_exp_f32_e32 v7, v7
	v_exp_f32_e32 v0, v0
	v_exp_f32_e32 v1, v1
	v_log_f32_e32 v21, v21
	v_pk_add_f32 v[6:7], v[6:7], 1.0 op_sel_hi:[1,0]
	v_log_f32_e32 v22, v22
	v_log_f32_e32 v6, v6
	v_log_f32_e32 v7, v7
	v_log_f32_e32 v23, v23
	s_nop 0
	s_nop 0
	v_exp_f32_e32 v4, v4
	v_exp_f32_e32 v5, v5
	v_lshl_or_b32 v42, v36, 5, v62
	v_exp_f32_e32 v2, v2
	v_exp_f32_e32 v3, v3
	v_cmp_eq_u32_e32 vcc, 0, v42
	v_pk_add_f32 v[0:1], v[0:1], 1.0 op_sel_hi:[1,0]
	v_pk_mul_f32 v[6:7], v[32:33], v[6:7] op_sel:[1,0]
	v_ashrrev_i32_e32 v43, 31, v42
	v_cndmask_b32_e64 v36, 0, 1, vcc
	v_log_f32_e32 v0, v0
	v_log_f32_e32 v1, v1
	v_cvt_pk_f16_f32 v55, v6, v7
	s_nop 0
	s_nop 0
	v_lshl_add_u64 v[44:45], v[42:43], 4, s[8:9]
	v_lshlrev_b32_e32 v36, 4, v36
	v_pk_mul_f32 v[16:17], v[32:33], v[16:17] op_sel:[1,0]
	v_pk_mul_f32 v[18:19], v[32:33], v[18:19] op_sel:[1,0]
	v_pk_mul_f32 v[20:21], v[32:33], v[20:21] op_sel:[1,0]
	v_pk_mul_f32 v[22:23], v[32:33], v[22:23] op_sel:[1,0]
	v_pk_add_f32 v[4:5], v[4:5], 1.0 op_sel_hi:[1,0]
	v_exp_f32_e32 v6, v10
	v_exp_f32_e32 v7, v11
	v_lshl_add_u64 v[38:39], v[44:45], 0, v[36:37]
	global_load_dwordx4 v[40:43], v[44:45], off
	global_load_dword v63, v[44:45], off offset:24
	global_load_dword v76, v[38:39], off offset:-8
	v_cvt_pk_f16_f32 v47, v22, v23
	v_cvt_pk_f16_f32 v46, v20, v21
	v_cvt_pk_f16_f32 v45, v18, v19
	v_cvt_pk_f16_f32 v44, v16, v17
	s_nop 0
	s_nop 0
	s_nop 0
	s_nop 0
	s_nop 0
	s_nop 0
	s_nop 0
	s_nop 0
	v_pk_add_f32 v[2:3], v[2:3], 1.0 op_sel_hi:[1,0]
	v_log_f32_e32 v4, v4
	v_log_f32_e32 v5, v5
	s_nop 0
	s_nop 0
	v_exp_f32_e32 v16, v24
	v_exp_f32_e32 v17, v25
	v_exp_f32_e32 v18, v26
	v_exp_f32_e32 v19, v27
	v_exp_f32_e32 v20, v28
	v_exp_f32_e32 v21, v29
	v_exp_f32_e32 v22, v30
	v_exp_f32_e32 v23, v31
	v_log_f32_e32 v2, v2
	v_log_f32_e32 v3, v3
	v_exp_f32_e32 v8, v8
	v_exp_f32_e32 v9, v9
	v_pk_mul_f32 v[0:1], v[32:33], v[0:1] op_sel:[1,0]
	v_pk_mul_f32 v[4:5], v[32:33], v[4:5] op_sel:[1,0]
	v_cvt_pk_f16_f32 v52, v0, v1
	v_pk_add_f32 v[0:1], v[6:7], 1.0 op_sel_hi:[1,0]
	v_pk_add_f32 v[16:17], v[16:17], 1.0 op_sel_hi:[1,0]
	v_log_f32_e32 v10, v0
	s_nop 0
	v_pk_add_f32 v[18:19], v[18:19], 1.0 op_sel_hi:[1,0]
	v_pk_add_f32 v[20:21], v[20:21], 1.0 op_sel_hi:[1,0]
	v_pk_add_f32 v[22:23], v[22:23], 1.0 op_sel_hi:[1,0]
	v_pk_mul_f32 v[2:3], v[32:33], v[2:3] op_sel:[1,0]
	v_cvt_pk_f16_f32 v54, v4, v5
	v_pk_add_f32 v[4:5], v[8:9], 1.0 op_sel_hi:[1,0]
	v_exp_f32_e32 v12, v12
	s_nop 0
	v_log_f32_e32 v16, v16
	v_log_f32_e32 v17, v17
	v_log_f32_e32 v18, v18
	v_log_f32_e32 v19, v19
	v_log_f32_e32 v20, v20
	v_log_f32_e32 v21, v21
	v_log_f32_e32 v22, v22
	v_log_f32_e32 v23, v23
	v_log_f32_e32 v4, v4
	v_log_f32_e32 v5, v5
	v_cvt_pk_f16_f32 v53, v2, v3
	v_log_f32_e32 v11, v1
	v_exp_f32_e32 v13, v13
	ds_read_b128 v[0:3], v68
	v_pk_mul_f32 v[16:17], v[32:33], v[16:17] op_sel:[1,0]
	v_pk_mul_f32 v[18:19], v[32:33], v[18:19] op_sel:[1,0]
	v_pk_mul_f32 v[20:21], v[32:33], v[20:21] op_sel:[1,0]
	v_pk_mul_f32 v[22:23], v[32:33], v[22:23] op_sel:[1,0]
	v_pk_mul_f32 v[8:9], v[32:33], v[4:5] op_sel:[1,0]
	s_nop 0
	v_cvt_pk_f16_f32 v51, v22, v23
	v_cvt_pk_f16_f32 v50, v20, v21
	v_cvt_pk_f16_f32 v49, v18, v19
	v_cvt_pk_f16_f32 v48, v16, v17
	v_exp_f32_e32 v14, v14
	ds_read_b128 v[4:7], v68 offset:1024
	s_waitcnt lgkmcnt(1)
	v_mfma_f32_32x32x16_f16 v[16:31], v[44:47], v[0:3], 0
	s_nop 0
	v_add_f32_e64 v0, v12, 1.0
	v_add_f32_e64 v1, v13, 1.0
	v_exp_f32_e32 v15, v15
	v_log_f32_e32 v0, v0
	v_log_f32_e32 v1, v1
	v_pk_mul_f32 v[10:11], v[32:33], v[10:11] op_sel:[1,0]
	v_pk_add_f32 v[2:3], v[14:15], 1.0 op_sel_hi:[1,0]
	s_waitcnt lgkmcnt(0)
	v_mfma_f32_32x32x16_f16 v[16:31], v[48:51], v[4:7], v[16:31]
	v_log_f32_e32 v12, v2
	v_log_f32_e32 v13, v3
	v_pk_mul_f32 v[4:5], v[32:33], v[0:1] op_sel:[1,0]
	ds_read_b128 v[0:3], v68 offset:2048
	v_cvt_pk_f16_f32 v82, v4, v5
	v_pk_mul_f32 v[6:7], v[32:33], v[12:13] op_sel:[1,0]
	v_cvt_pk_f16_f32 v81, v10, v11
	v_cvt_pk_f16_f32 v83, v6, v7
	ds_read_b128 v[4:7], v68 offset:3072
	s_waitcnt lgkmcnt(1)
	v_mfma_f32_32x32x16_f16 v[16:31], v[52:55], v[0:3], v[16:31]
	v_cvt_pk_f16_f32 v80, v8, v9
	v_cvt_f16_f32_e32 v0, v33
	v_mov_b32_e32 v38, v37
	v_mov_b32_e32 v39, v37
	ds_read_b128 v[84:87], v69 offset:1024
	v_cndmask_b32_e64 v0, 0, v0, s[0:1]
	v_pack_b32_f16 v36, v0, 0
	s_waitcnt lgkmcnt(1)
	v_mfma_f32_32x32x16_f16 v[16:31], v[80:83], v[4:7], v[16:31]
	ds_read_b128 v[0:3], v69
	ds_read_b128 v[88:91], v68 offset:5120
	s_ashr_i32 s17, s21, 9
	v_readlane_b32 s22, v35, 1
	s_and_b32 s17, s17, 0xffffff80
	v_or_b32_e32 v32, s17, v70
	s_ashr_i32 s17, s22, 9
	s_waitcnt lgkmcnt(1)
	v_mfma_f32_32x32x16_f16 v[16:31], v[36:39], v[0:3], v[16:31]
	ds_read_b128 v[0:3], v68 offset:4096
	v_readlane_b32 s23, v35, 2
	s_and_b32 s17, s17, 0xffffff80
	v_or_b32_e32 v33, s17, v70
	s_ashr_i32 s17, s23, 9
	v_readlane_b32 s24, v35, 3
	s_and_b32 s17, s17, 0xffffff80
	s_waitcnt lgkmcnt(0)
	v_mfma_f32_32x32x16_f16 v[0:15], v[44:47], v[0:3], 0
	ds_read_b128 v[44:47], v68 offset:6144
	v_readlane_b32 s25, v35, 4
	v_readlane_b32 s26, v35, 5
	v_readlane_b32 s27, v35, 6
	v_readlane_b32 s28, v35, 7
	v_readlane_b32 s29, v35, 8
	v_readlane_b32 s30, v35, 9
	v_mfma_f32_32x32x16_f16 v[0:15], v[48:51], v[88:91], v[0:15]
	ds_read_b128 v[48:51], v68 offset:7168
	v_readlane_b32 s31, v35, 10
	v_readlane_b32 s33, v35, 11
	v_readlane_b32 s34, v35, 12
	v_readlane_b32 s35, v35, 13
	v_readlane_b32 s36, v35, 14
	v_readlane_b32 s37, v35, 15
	s_waitcnt lgkmcnt(1)
	v_mfma_f32_32x32x16_f16 v[0:15], v[52:55], v[44:47], v[0:15]
	v_readlane_b32 s38, v35, 16
	v_readlane_b32 s39, v35, 17
	v_readlane_b32 s40, v35, 18
	v_readlane_b32 s41, v35, 19
	v_readlane_b32 s42, v35, 20
	v_readlane_b32 s43, v35, 21
	v_readlane_b32 s44, v35, 22
	s_waitcnt lgkmcnt(0)
	v_mfma_f32_32x32x16_f16 v[0:15], v[80:83], v[48:51], v[0:15]
	v_readlane_b32 s45, v35, 23
	v_readlane_b32 s46, v35, 24
	v_readlane_b32 s47, v35, 25
	v_readlane_b32 s48, v35, 26
	v_readlane_b32 s49, v35, 27
	v_readlane_b32 s50, v35, 28
	v_readlane_b32 s51, v35, 29
	v_readlane_b32 s52, v35, 30
	v_readlane_b32 s4, v35, 31
	v_or_b32_e32 v35, s17, v70
	s_ashr_i32 s17, s24, 9
	s_and_b32 s17, s17, 0xffffff80
	v_mfma_f32_32x32x16_f16 v[0:15], v[36:39], v[84:87], v[0:15]
	v_or_b32_e32 v36, s17, v70
	s_ashr_i32 s17, s25, 9
	s_and_b32 s17, s17, 0xffffff80
	v_or_b32_e32 v38, s17, v70
	s_ashr_i32 s17, s26, 9
	s_and_b32 s17, s17, 0xffffff80
	v_or_b32_e32 v39, s17, v70
	s_ashr_i32 s17, s27, 9
	s_and_b32 s17, s17, 0xffffff80
	v_or_b32_e32 v44, s17, v70
	s_ashr_i32 s17, s28, 9
	s_and_b32 s17, s17, 0xffffff80
	v_or_b32_e32 v45, s17, v70
	s_ashr_i32 s17, s29, 9
	s_and_b32 s17, s17, 0xffffff80
	ds_read_u16 v32, v32
	ds_read_u16 v91, v33
	ds_read_u16 v90, v35
	ds_read_u16 v89, v36
	ds_read_u16 v88, v38
	ds_read_u16 v87, v39
	ds_read_u16 v86, v44
	ds_read_u16 v85, v45
	v_or_b32_e32 v33, s17, v70
	s_ashr_i32 s17, s30, 9
	s_and_b32 s17, s17, 0xffffff80
	v_or_b32_e32 v35, s17, v70
	s_ashr_i32 s17, s31, 9
	s_and_b32 s17, s17, 0xffffff80
	v_or_b32_e32 v36, s17, v70
	s_ashr_i32 s17, s33, 9
	s_and_b32 s17, s17, 0xffffff80
	v_or_b32_e32 v38, s17, v70
	s_ashr_i32 s17, s34, 9
	s_and_b32 s17, s17, 0xffffff80
	v_or_b32_e32 v39, s17, v70
	s_ashr_i32 s17, s35, 9
	s_and_b32 s17, s17, 0xffffff80
	v_or_b32_e32 v44, s17, v70
	s_ashr_i32 s17, s36, 9
	s_and_b32 s17, s17, 0xffffff80
	v_or_b32_e32 v45, s17, v70
	s_ashr_i32 s17, s37, 9
	s_and_b32 s17, s17, 0xffffff80
	v_or_b32_e32 v46, s17, v70
	s_ashr_i32 s17, s38, 9
	s_and_b32 s17, s17, 0xffffff80
	v_cmp_ne_u32_sdwa s[18:19], v77, v34 src0_sel:DWORD src1_sel:WORD_1
	ds_read_u16 v84, v33
	ds_read_u16 v83, v35
	ds_read_u16 v82, v36
	ds_read_u16 v81, v38
	ds_read_u16 v80, v39
	ds_read_u16 v79, v44
	ds_read_u16 v78, v45
	ds_read_u16 v77, v46
	v_or_b32_e32 v33, s17, v70
	s_ashr_i32 s17, s39, 9
	s_and_b32 s17, s17, 0xffffff80
	v_or_b32_e32 v35, s17, v70
	s_ashr_i32 s17, s40, 9
	s_and_b32 s17, s17, 0xffffff80
	v_or_b32_e32 v36, s17, v70
	s_ashr_i32 s17, s41, 9
	s_and_b32 s17, s17, 0xffffff80
	v_or_b32_e32 v38, s17, v70
	s_ashr_i32 s17, s42, 9
	s_and_b32 s17, s17, 0xffffff80
	v_or_b32_e32 v39, s17, v70
	s_ashr_i32 s17, s43, 9
	s_and_b32 s17, s17, 0xffffff80
	v_or_b32_e32 v44, s17, v70
	s_ashr_i32 s17, s44, 9
	s_and_b32 s17, s17, 0xffffff80
	v_or_b32_e32 v45, s17, v70
	s_ashr_i32 s17, s45, 9
	s_and_b32 s17, s17, 0xffffff80
	v_or_b32_e32 v46, s17, v70
	s_ashr_i32 s17, s46, 9
	s_and_b32 s17, s17, 0xffffff80
	ds_read_u16 v55, v33
	ds_read_u16 v54, v35
	ds_read_u16 v53, v36
	ds_read_u16 v52, v38
	ds_read_u16 v51, v39
	ds_read_u16 v50, v44
	ds_read_u16 v49, v45
	ds_read_u16 v48, v46
	v_or_b32_e32 v33, s17, v70
	s_ashr_i32 s17, s47, 9
	s_and_b32 s17, s17, 0xffffff80
	v_or_b32_e32 v35, s17, v70
	s_ashr_i32 s17, s48, 9
	s_and_b32 s17, s17, 0xffffff80
	v_or_b32_e32 v36, s17, v70
	s_ashr_i32 s17, s49, 9
	s_and_b32 s17, s17, 0xffffff80
	v_or_b32_e32 v38, s17, v70
	s_ashr_i32 s17, s50, 9
	s_and_b32 s17, s17, 0xffffff80
	v_or_b32_e32 v39, s17, v70
	s_ashr_i32 s17, s51, 9
	s_and_b32 s17, s17, 0xffffff80
	v_or_b32_e32 v92, s17, v70
	s_ashr_i32 s17, s52, 9
	s_and_b32 s17, s17, 0xffffff80
	v_or_b32_e32 v93, s17, v70
	ds_read_u16 v47, v33
	ds_read_u16 v46, v35
	ds_read_u16 v45, v36
	ds_read_u16 v44, v38
	ds_read_u16 v39, v39
	ds_read_u16 v38, v92
	ds_read_u16 v36, v93
	s_ashr_i32 s4, s4, 9
	s_and_b32 s4, s4, 0xffffff80
	s_waitcnt lgkmcnt(14)
	v_cvt_f32_f16_e32 v32, v32
	v_or_b32_e32 v33, s4, v70
	ds_read_u16 v35, v33
	s_waitcnt vmcnt(0)
	v_permlane32_swap_b32_e32 v16, v0
	s_bitcmp1_b32 s18, 0
	v_mul_f32_e32 v32, v16, v32
	v_mov_b32_e32 v33, v16
	v_cmp_lt_i32_e64 s[2:3], s7, v56
	v_permlane32_swap_b32_e32 v17, v1
	v_permlane32_swap_b32_e32 v18, v2
	v_permlane32_swap_b32_e32 v19, v3
	v_permlane32_swap_b32_e32 v20, v4
	v_permlane32_swap_b32_e32 v21, v5
	v_permlane32_swap_b32_e32 v22, v6
	v_permlane32_swap_b32_e32 v23, v7
	v_permlane32_swap_b32_e32 v24, v8
	v_permlane32_swap_b32_e32 v25, v9
	v_permlane32_swap_b32_e32 v26, v10
	v_permlane32_swap_b32_e32 v27, v11
	v_permlane32_swap_b32_e32 v28, v12
	v_permlane32_swap_b32_e32 v29, v13
	v_permlane32_swap_b32_e32 v30, v14
	v_permlane32_swap_b32_e32 v31, v15
	s_cselect_b64 s[18:19], -1, 0
	s_bitcmp0_b32 s16, 0
	v_pk_add_f32 v[32:33], v[32:33], 0 op_sel_hi:[1,0]
	s_cbranch_scc1 .LBB3_13
	v_readlane_b32 s4, v34, 0
	s_bfe_u32 s17, s4, 0x80008
	v_lshl_or_b32 v16, s17, 7, v70
	ds_read_u16 v16, v16
	s_bfe_u32 s4, s4, 0x100010
	s_lshl_b32 s4, s4, 8
	v_lshl_add_u64 v[92:93], v[58:59], 0, s[4:5]
	v_cndmask_b32_e64 v93, v61, v93, s[18:19]
	s_waitcnt lgkmcnt(0)
	v_fma_mix_f32 v16, v16, v33, v32 op_sel_hi:[1,0,0]
	v_mov_b32_e32 v32, 0
	v_cndmask_b32_e64 v92, v60, v92, s[18:19]
	s_mov_b64 s[18:19], -1
	v_mov_b32_e32 v33, v32
	global_store_dword v[92:93], v16, off sc1

.LBB4_8:
	s_or_b64 exec, exec, s[2:3]
	s_movk_i32 s17, 0x61a8
	v_cmp_gt_i32_e32 vcc, s17, v64
	s_waitcnt lgkmcnt(0)
	s_barrier
	s_and_saveexec_b64 s[2:3], vcc
	s_cbranch_execz .LBB4_73
	s_load_dwordx4 s[4:7], s[0:1], 0x30
	s_load_dwordx2 s[2:3], s[0:1], 0x40
	v_and_b32_e32 v1, 63, v0
	s_waitcnt vmcnt(3)
	v_mov_b32_e32 v2, 0x3e020821
	v_cmp_gt_u32_e64 s[0:1], 32, v1
	v_mov_b32_e32 v68, 0xffff
	v_cmp_ne_u32_e32 vcc, 0, v54
	v_cndmask_b32_e64 v67, v2, 0, s[0:1]
	s_waitcnt vmcnt(0)
	v_lshrrev_b32_e32 v2, 16, v55
	v_lshrrev_b32_e32 v0, 1, v0
	v_mov_b32_e32 v3, 0x7a00
	v_ashrrev_i32_e32 v65, 31, v64
	v_lshlrev_b32_e32 v52, 2, v1
	v_cndmask_b32_e32 v95, v68, v2, vcc
	s_lshl_b32 s12, s10, 2
	v_lshlrev_b32_e32 v2, 4, v1
	v_and_or_b32 v70, v0, 16, v3
	v_lshlrev_b32_e32 v73, 1, v1
	v_lshlrev_b64 v[0:1], 8, v[64:65]
	v_mov_b32_e32 v53, 0
	v_or_b32_e32 v0, v0, v52
	s_ashr_i32 s13, s12, 31
	s_mov_b32 s11, 0
	v_add_u32_e32 v69, 0x3200, v2
	v_add_u32_e32 v71, 0x5200, v2
	v_add_u32_e32 v72, 0x7200, v2
	s_waitcnt lgkmcnt(0)
	v_lshl_add_u64 v[60:61], s[6:7], 0, v[52:53]
	v_lshl_add_u64 v[62:63], s[2:3], 0, v[0:1]
	s_lshl_b64 s[6:7], s[12:13], 8
	s_mov_b64 s[14:15], 0
	s_movk_i32 s13, 0x61a7
	v_mov_b32_e32 v65, 0xc0669d92
	s_mov_b32 s22, 0xc1c00000
	v_mov_b32_e32 v74, 0x41c00000
	v_mov_b32_e32 v75, 0xbfb8aa3b
	v_mov_b32_e32 v76, 0xc1b69213
	v_mov_b32_e32 v77, 0xc228283a
	v_mov_b32_e32 v78, 0xc275076b
	s_mov_b32 s16, 0x3e0a9555
	v_mov_b32_e32 v79, v52
	v_readfirstlane_b32 s94, v64
	s_nop 3
	s_branch .LBB4_11

.Lprio_e1_done:
	s_add_u32 s94, s94, 0x1000
	v_sub_f32_e32 v39, v48, v67
	v_fmamk_f32 v32, v39, 0x4297576a, v65
	v_fmamk_f32 v33, v39, 0x4297576a, v76
	v_med3_f32 v35, v32, s22, v74
	v_med3_f32 v37, v33, s22, v74
	v_mul_f32_e64 v32, v35, -v35
	v_fmamk_f32 v34, v35, 0x4019be61, v75
	v_mul_f32_e64 v33, v37, -v37
	v_fmamk_f32 v35, v35, 0xc019be61, v75
	v_exp_f32_e32 v32, v32
	v_exp_f32_e32 v33, v33
	v_exp_f32_e32 v36, v35
	v_fmamk_f32 v35, v37, 0x4019be61, v75
	v_exp_f32_e32 v34, v34
	v_exp_f32_e32 v35, v35
	v_fmamk_f32 v37, v37, 0xc019be61, v75
	v_exp_f32_e32 v37, v37
	v_pk_mul_f32 v[32:33], v[48:49], v[32:33] op_sel:[1,0]
	ds_read_b128 v[28:31], v69
	ds_read_b128 v[24:27], v69 offset:1024
	ds_read_b128 v[20:23], v69 offset:2048
	ds_read_b128 v[16:19], v69 offset:3072
	ds_read_b128 v[0:3], v70
	ds_read_b128 v[4:7], v70 offset:32
	ds_read_b128 v[8:11], v70 offset:64
	ds_read_b128 v[12:15], v70 offset:96
	v_pk_mul_f32 v[44:45], v[34:35], v[32:33]
	v_pk_mul_f32 v[34:35], v[34:35], s[16:17] op_sel_hi:[1,0]
	v_mov_b32_e32 v99, v80
	v_fmamk_f32 v38, v39, 0x4297576a, v77
	v_fmamk_f32 v39, v39, 0x4297576a, v78
	v_pk_mul_f32 v[46:47], v[34:35], v[44:45]
	v_pk_mul_f32 v[34:35], v[34:35], s[16:17] op_sel_hi:[1,0]
	v_pk_mul_f32 v[80:81], v[36:37], v[32:33]
	v_pk_mul_f32 v[36:37], v[36:37], s[16:17] op_sel_hi:[1,0]
	v_med3_f32 v41, v38, s22, v74
	v_med3_f32 v43, v39, s22, v74
	v_pk_mul_f32 v[58:59], v[34:35], v[46:47]
	v_pk_mul_f32 v[34:35], v[34:35], s[16:17] op_sel_hi:[1,0]
	v_pk_mul_f32 v[82:83], v[36:37], v[80:81]
	v_pk_mul_f32 v[36:37], v[36:37], s[16:17] op_sel_hi:[1,0]
	v_mul_f32_e64 v38, v41, -v41
	v_fmamk_f32 v40, v41, 0x4019be61, v75
	v_mul_f32_e64 v39, v43, -v43
	v_fmamk_f32 v41, v41, 0xc019be61, v75
	v_pk_mul_f32 v[34:35], v[34:35], v[58:59]
	v_pk_mul_f32 v[36:37], v[36:37], v[82:83]
	v_exp_f32_e32 v38, v38
	v_exp_f32_e32 v39, v39
	v_exp_f32_e32 v42, v41
	v_fmamk_f32 v41, v43, 0x4019be61, v75
	v_cvt_pk_f16_f32 v56, v44, v46
	v_cvt_pk_f16_f32 v54, v36, v82
	v_cvt_pk_f16_f32 v57, v58, v34
	v_cvt_pk_f16_f32 v55, v80, v32
	v_exp_f32_e32 v40, v40
	v_exp_f32_e32 v41, v41
	s_waitcnt lgkmcnt(0)
	v_mfma_f32_32x32x16_f16 v[0:15], v[28:31], v[54:57], v[0:15]
	v_mul_f32_e64 v38, v49, v38
	v_mul_f32_e64 v39, v49, v39
	v_fmamk_f32 v43, v43, 0xc019be61, v75
	v_mul_f32_e64 v84, v40, v38
	v_mul_f32_e64 v85, v41, v39
	v_pk_mul_f32 v[40:41], v[40:41], s[16:17] op_sel_hi:[1,0]
	v_cvt_pk_f16_f32 v30, v45, v47
	v_pk_mul_f32 v[86:87], v[40:41], v[84:85]
	v_pk_mul_f32 v[28:29], v[40:41], s[16:17] op_sel_hi:[1,0]
	v_cvt_pk_f16_f32 v31, v59, v35
	v_pk_mul_f32 v[40:41], v[28:29], v[86:87]
	v_pk_mul_f32 v[28:29], v[28:29], s[16:17] op_sel_hi:[1,0]
	v_exp_f32_e32 v43, v43
	v_pk_mul_f32 v[88:89], v[28:29], v[40:41]
	v_cvt_pk_f16_f32 v28, v37, v83
	v_cvt_pk_f16_f32 v29, v81, v33
	v_pk_mul_f32 v[36:37], v[42:43], v[38:39]
	v_pk_mul_f32 v[42:43], v[42:43], s[16:17] op_sel_hi:[1,0]
	v_mfma_f32_32x32x16_f16 v[0:15], v[24:27], v[28:31], v[0:15]
	v_mul_f32_e64 v32, v42, v36
	v_mul_f32_e64 v33, v43, v37
	v_mul_f32_e64 v24, v42, s16
	v_mul_f32_e64 v25, v43, s16
	v_cvt_pk_f16_f32 v26, v84, v86
	v_pk_mul_f32 v[34:35], v[24:25], v[32:33]
	v_cvt_pk_f16_f32 v27, v40, v88
	v_cvt_pk_f16_f32 v24, v34, v32
	v_cvt_pk_f16_f32 v25, v36, v38
	v_cvt_pk_f16_f32 v84, v85, v87
	v_cvt_pk_f16_f32 v82, v35, v33
	v_mfma_f32_32x32x16_f16 v[0:15], v[20:23], v[24:27], v[0:15]
	ds_read_b128 v[20:23], v69 offset:4096
	v_cvt_pk_f16_f32 v85, v41, v89
	v_cvt_pk_f16_f32 v83, v37, v39
	ds_read_b128 v[32:35], v70 offset:128
	ds_read_b128 v[36:39], v70 offset:160
	ds_read_b128 v[40:43], v70 offset:192
	ds_read_b128 v[44:47], v70 offset:224
	v_mov_b32_e32 v52, v64
	v_add_u32_e32 v64, s12, v52
	v_readlane_b32 s48, v51, 0
	v_mfma_f32_32x32x16_f16 v[0:15], v[16:19], v[82:85], v[0:15]
	ds_read_b128 v[16:19], v69 offset:5120
	v_cmp_gt_i32_e32 vcc, s17, v64
	s_lshl_b32 s48, s48, 8
	s_and_b32 s48, s48, 0xffff00
	v_readlane_b32 s47, v51, 1
	s_add_u32 s48, s4, s48
	s_addc_u32 s49, s5, 0
	s_waitcnt lgkmcnt(1)
	v_mfma_f32_32x32x16_f16 v[32:47], v[20:23], v[54:57], v[32:47]
	ds_read_b128 v[20:23], v69 offset:6144
	s_lshl_b32 s47, s47, 8
	s_and_b32 s47, s47, 0xffff00
	v_readlane_b32 s46, v51, 2
	v_readlane_b32 s45, v51, 3
	v_readlane_b32 s44, v51, 4
	v_readlane_b32 s43, v51, 5
	s_waitcnt lgkmcnt(1)
	v_mfma_f32_32x32x16_f16 v[32:47], v[16:19], v[28:31], v[32:47]
	v_cndmask_b32_e32 v16, v52, v64, vcc
	v_lshl_or_b32 v28, v16, 5, v66
	v_cmp_eq_u32_e32 vcc, 0, v28
	v_ashrrev_i32_e32 v29, 31, v28
	v_lshl_add_u64 v[30:31], v[28:29], 4, s[8:9]
	v_readlane_b32 s3, v51, 6
	v_readlane_b32 s2, v51, 7
	s_waitcnt lgkmcnt(0)
	v_mfma_f32_32x32x16_f16 v[32:47], v[20:23], v[24:27], v[32:47]
	v_cndmask_b32_e64 v20, 0, 1, vcc
	v_lshlrev_b32_e32 v52, 4, v20
	v_readlane_b32 s36, v51, 8
	v_readlane_b32 s35, v51, 9
	v_readlane_b32 s34, v51, 10
	v_readlane_b32 s33, v51, 11
	v_readlane_b32 s31, v51, 12
	v_readlane_b32 s30, v51, 13
	v_readlane_b32 s29, v51, 14
	v_readlane_b32 s28, v51, 15
	v_readlane_b32 s27, v51, 16
	v_readlane_b32 s26, v51, 17
	v_readlane_b32 s25, v51, 18
	v_readlane_b32 s24, v51, 19
	v_readlane_b32 s23, v51, 20
	v_readlane_b32 s42, v51, 21
	v_readlane_b32 s41, v51, 22
	v_readlane_b32 s40, v51, 23
	v_readlane_b32 s39, v51, 24
	v_readlane_b32 s38, v51, 25
	v_readlane_b32 s37, v51, 26
	v_readlane_b32 s21, v51, 27
	v_readlane_b32 s20, v51, 28
	v_readlane_b32 s19, v51, 29
	v_readlane_b32 s18, v51, 30
	v_readlane_b32 s10, v51, 31
	ds_read_b128 v[16:19], v69 offset:7168
	v_lshl_add_u64 v[20:21], v[30:31], 0, v[52:53]
	global_load_dwordx4 v[56:59], v[30:31], off
	global_load_dword v80, v[30:31], off offset:24
	global_load_dword v51, v[20:21], off offset:-8
	global_load_dword v112, v79, s[48:49]
	s_add_u32 s48, s4, s47
	s_addc_u32 s49, s5, 0
	s_lshl_b32 s46, s46, 8
	s_and_b32 s46, s46, 0xffff00
	s_add_u32 s46, s4, s46
	s_addc_u32 s47, s5, 0
	s_lshl_b32 s45, s45, 8
	s_and_b32 s45, s45, 0xffff00
	global_load_dword v110, v79, s[48:49]
	global_load_dword v108, v79, s[46:47]
	s_add_u32 s46, s4, s45
	s_addc_u32 s47, s5, 0
	s_lshl_b32 s44, s44, 8
	s_and_b32 s44, s44, 0xffff00
	s_add_u32 s44, s4, s44
	s_addc_u32 s45, s5, 0
	s_lshl_b32 s43, s43, 8
	s_and_b32 s43, s43, 0xffff00
	global_load_dword v106, v79, s[46:47]
	global_load_dword v104, v79, s[44:45]
	s_add_u32 s44, s4, s43
	s_addc_u32 s45, s5, 0
	s_lshl_b32 s3, s3, 8
	s_and_b32 s3, s3, 0xffff00
	global_load_dword v102, v79, s[44:45]
	s_add_u32 s44, s4, s3
	s_addc_u32 s45, s5, 0
	s_lshl_b32 s2, s2, 8
	s_and_b32 s2, s2, 0xffff00
	s_add_u32 s2, s4, s2
	global_load_dword v100, v79, s[44:45]
	s_addc_u32 s3, s5, 0
	global_load_dword v114, v79, s[2:3]
	s_lshl_b32 s2, s36, 8
	s_and_b32 s2, s2, 0xffff00
	s_add_u32 s2, s4, s2
	s_addc_u32 s3, s5, 0
	global_load_dword v113, v79, s[2:3]
	s_lshl_b32 s2, s35, 8
	s_and_b32 s2, s2, 0xffff00
	s_add_u32 s2, s4, s2
	s_addc_u32 s3, s5, 0
	global_load_dword v111, v79, s[2:3]
	s_lshl_b32 s2, s34, 8
	s_and_b32 s2, s2, 0xffff00
	s_add_u32 s2, s4, s2
	s_addc_u32 s3, s5, 0
	global_load_dword v109, v79, s[2:3]
	s_lshl_b32 s2, s33, 8
	s_and_b32 s2, s2, 0xffff00
	s_add_u32 s2, s4, s2
	s_addc_u32 s3, s5, 0
	global_load_dword v107, v79, s[2:3]
	s_lshl_b32 s2, s31, 8
	s_and_b32 s2, s2, 0xffff00
	s_add_u32 s2, s4, s2
	s_addc_u32 s3, s5, 0
	global_load_dword v105, v79, s[2:3]
	s_lshl_b32 s2, s30, 8
	s_and_b32 s2, s2, 0xffff00
	s_add_u32 s2, s4, s2
	s_addc_u32 s3, s5, 0
	global_load_dword v103, v79, s[2:3]
	s_lshl_b32 s2, s29, 8
	s_and_b32 s2, s2, 0xffff00
	s_add_u32 s2, s4, s2
	s_addc_u32 s3, s5, 0
	global_load_dword v101, v79, s[2:3]
	s_lshl_b32 s2, s28, 8
	s_and_b32 s2, s2, 0xffff00
	s_add_u32 s2, s4, s2
	s_addc_u32 s3, s5, 0
	global_load_dword v98, v79, s[2:3]
	s_lshl_b32 s2, s27, 8
	s_and_b32 s2, s2, 0xffff00
	s_add_u32 s2, s4, s2
	s_addc_u32 s3, s5, 0
	global_load_dword v97, v79, s[2:3]
	s_lshl_b32 s2, s26, 8
	s_and_b32 s2, s2, 0xffff00
	s_add_u32 s2, s4, s2
	s_addc_u32 s3, s5, 0
	global_load_dword v96, v79, s[2:3]
	s_lshl_b32 s2, s25, 8
	s_and_b32 s2, s2, 0xffff00
	s_add_u32 s2, s4, s2
	s_addc_u32 s3, s5, 0
	global_load_dword v94, v79, s[2:3]
	s_lshl_b32 s2, s24, 8
	s_and_b32 s2, s2, 0xffff00
	s_add_u32 s2, s4, s2
	s_addc_u32 s3, s5, 0
	global_load_dword v91, v79, s[2:3]
	s_lshl_b32 s2, s23, 8
	s_and_b32 s2, s2, 0xffff00
	s_add_u32 s2, s4, s2
	s_addc_u32 s3, s5, 0
	global_load_dword v93, v79, s[2:3]
	s_lshl_b32 s2, s42, 8
	s_and_b32 s2, s2, 0xffff00
	s_add_u32 s2, s4, s2
	s_addc_u32 s3, s5, 0
	global_load_dword v90, v79, s[2:3]
	s_lshl_b32 s2, s41, 8
	s_and_b32 s2, s2, 0xffff00
	s_add_u32 s2, s4, s2
	s_addc_u32 s3, s5, 0
	global_load_dword v88, v79, s[2:3]
	s_lshl_b32 s2, s40, 8
	s_and_b32 s2, s2, 0xffff00
	s_add_u32 s2, s4, s2
	s_addc_u32 s3, s5, 0
	global_load_dword v86, v79, s[2:3]
	s_lshl_b32 s2, s39, 8
	s_and_b32 s2, s2, 0xffff00
	s_nop 0
	s_nop 0
	s_add_u32 s2, s4, s2
	s_waitcnt lgkmcnt(0)
	v_mfma_f32_32x32x16_f16 v[32:47], v[16:19], v[82:85], v[32:47]
	v_exp_f32_e32 v0, v0
	v_exp_f32_e32 v1, v1
	s_addc_u32 s3, s5, 0
	global_load_dword v85, v79, s[2:3]
	s_lshl_b32 s2, s38, 8
	s_and_b32 s2, s2, 0xffff00
	s_nop 0
	s_nop 0
	s_add_u32 s2, s4, s2
	v_exp_f32_e32 v6, v6
	v_exp_f32_e32 v7, v7
	s_addc_u32 s3, s5, 0
	global_load_dword v83, v79, s[2:3]
	s_lshl_b32 s2, s37, 8
	v_pk_add_f32 v[0:1], v[0:1], 1.0 op_sel_hi:[1,0]
	s_and_b32 s2, s2, 0xffff00
	s_nop 0
	s_nop 0
	v_min_f32 v16, 0x42fc0000, v4
	v_min_f32 v17, 0x42fc0000, v5
	v_log_f32_e32 v4, v0
	v_log_f32_e32 v5, v1
	v_exp_f32_e32 v0, v16
	v_exp_f32_e32 v1, v17
	s_add_u32 s2, s4, s2
	v_exp_f32_e32 v2, v2
	v_exp_f32_e32 v3, v3
	s_addc_u32 s3, s5, 0
	global_load_dword v92, v79, s[2:3]
	s_lshl_b32 s2, s21, 8
	v_pk_add_f32 v[6:7], v[6:7], 1.0 op_sel_hi:[1,0]
	s_and_b32 s2, s2, 0xffff00
	v_log_f32_e32 v6, v6
	v_log_f32_e32 v7, v7
	s_add_u32 s2, s4, s2
	v_pk_add_f32 v[0:1], v[0:1], 1.0 op_sel_hi:[1,0]
	s_addc_u32 s3, s5, 0
	global_load_dword v89, v79, s[2:3]
	s_lshl_b32 s2, s20, 8
	v_pk_add_f32 v[2:3], v[2:3], 1.0 op_sel_hi:[1,0]
	v_log_f32_e32 v0, v0
	v_log_f32_e32 v1, v1
	s_and_b32 s2, s2, 0xffff00
	v_min_f32 v18, 0x42fc0000, v8
	v_min_f32 v19, 0x42fc0000, v9
	v_log_f32_e32 v8, v2
	v_log_f32_e32 v9, v3
	s_add_u32 s2, s4, s2
	v_pk_mul_f32 v[2:3], v[48:49], v[6:7] op_sel:[1,0]
	v_exp_f32_e32 v6, v18
	v_exp_f32_e32 v7, v19
	s_addc_u32 s3, s5, 0
	s_lshl_b32 s19, s19, 8
	s_and_b32 s19, s19, 0xffff00
	v_pk_mul_f32 v[0:1], v[48:49], v[0:1] op_sel:[1,0]
	s_add_u32 s20, s4, s19
	s_nop 0
	s_nop 0
	v_cvt_pk_f16_f32 v3, v2, v3
	v_cvt_pk_f16_f32 v2, v0, v1
	v_pk_mul_f32 v[0:1], v[48:49], v[8:9] op_sel:[1,0]
	v_pk_mul_f32 v[4:5], v[48:49], v[4:5] op_sel:[1,0]
	s_addc_u32 s21, s5, 0
	s_lshl_b32 s18, s18, 8
	s_nop 0
	s_nop 0
	s_nop 0
	s_nop 0
	v_cvt_pk_f16_f32 v1, v0, v1
	v_cvt_pk_f16_f32 v0, v4, v5
	v_pk_add_f32 v[4:5], v[6:7], 1.0 op_sel_hi:[1,0]
	v_exp_f32_e32 v6, v10
	v_exp_f32_e32 v7, v11
	v_exp_f32_e32 v8, v12
	v_exp_f32_e32 v9, v13
	v_exp_f32_e32 v10, v14
	v_exp_f32_e32 v11, v15
	s_and_b32 s18, s18, 0xffff00
	s_add_u32 s18, s4, s18
	s_addc_u32 s19, s5, 0
	s_lshl_b32 s10, s10, 8
	s_and_b32 s10, s10, 0xffff00
	v_pk_add_f32 v[8:9], v[8:9], 1.0 op_sel_hi:[1,0]
	v_pk_add_f32 v[10:11], v[10:11], 1.0 op_sel_hi:[1,0]
	s_add_u32 s24, s4, s10
	v_pk_add_f32 v[6:7], v[6:7], 1.0 op_sel_hi:[1,0]
	v_log_f32_e32 v8, v8
	v_log_f32_e32 v9, v9
	v_log_f32_e32 v10, v10
	v_log_f32_e32 v11, v11
	s_addc_u32 s25, s5, 0
	global_load_dword v87, v79, s[2:3]
	global_load_dword v84, v79, s[20:21]
	global_load_dword v82, v79, s[18:19]
	global_load_dword v81, v79, s[24:25]
	ds_read_b128 v[12:15], v71
	v_log_f32_e32 v6, v6
	v_log_f32_e32 v7, v7
	v_log_f32_e32 v4, v4
	v_log_f32_e32 v5, v5
	v_pk_mul_f32 v[8:9], v[48:49], v[8:9] op_sel:[1,0]
	v_pk_mul_f32 v[10:11], v[48:49], v[10:11] op_sel:[1,0]
	v_cvt_pk_f16_f32 v118, v8, v9
	v_cvt_pk_f16_f32 v119, v10, v11
	v_pk_mul_f32 v[10:11], v[48:49], v[6:7] op_sel:[1,0]
	ds_read_b128 v[6:9], v71 offset:1024
	s_waitcnt lgkmcnt(1)
	v_mfma_f32_32x32x16_f16 v[16:31], v[0:3], v[12:15], 0
	s_nop 0
	s_nop 0
	v_mul_f32_e64 v4, v49, v4
	v_mul_f32_e64 v5, v49, v5
	v_exp_f32_e32 v32, v32
	v_exp_f32_e32 v33, v33
	s_nop 0
	s_nop 0
	v_cvt_pk_f16_f32 v117, v10, v11
	v_cvt_pk_f16_f32 v116, v4, v5
	v_exp_f32_e32 v36, v36
	v_exp_f32_e32 v37, v37
	v_pk_add_f32 v[32:33], v[32:33], 1.0 op_sel_hi:[1,0]
	s_waitcnt lgkmcnt(0)
	v_mfma_f32_32x32x16_f16 v[16:31], v[116:119], v[6:9], v[16:31]
	v_log_f32_e32 v54, v32
	v_log_f32_e32 v55, v33
	v_pk_add_f32 v[32:33], v[36:37], 1.0 op_sel_hi:[1,0]
	s_nop 0
	s_nop 0
	ds_read_b128 v[4:7], v71 offset:4096
	ds_read_b128 v[120:123], v71 offset:5120
	v_exp_f32_e32 v36, v38
	v_exp_f32_e32 v37, v39
	s_nop 0
	s_nop 0
	s_waitcnt lgkmcnt(1)
	v_mfma_f32_32x32x16_f16 v[0:15], v[0:3], v[4:7], 0
	v_exp_f32_e32 v34, v34
	v_exp_f32_e32 v35, v35
	v_pk_add_f32 v[36:37], v[36:37], 1.0 op_sel_hi:[1,0]
	v_log_f32_e32 v32, v32
	v_log_f32_e32 v33, v33
	v_log_f32_e32 v36, v36
	v_log_f32_e32 v37, v37
	v_pk_add_f32 v[34:35], v[34:35], 1.0 op_sel_hi:[1,0]
	v_pk_mul_f32 v[32:33], v[48:49], v[32:33] op_sel:[1,0]
	v_log_f32_e32 v38, v34
	v_log_f32_e32 v39, v35
	v_pk_mul_f32 v[34:35], v[48:49], v[36:37] op_sel:[1,0]
	v_pk_mul_f32 v[36:37], v[48:49], v[54:55] op_sel:[1,0]
	v_cvt_pk_f16_f32 v35, v34, v35
	v_cvt_pk_f16_f32 v34, v32, v33
	v_pk_mul_f32 v[32:33], v[48:49], v[38:39] op_sel:[1,0]
	s_waitcnt lgkmcnt(0)
	v_mfma_f32_32x32x16_f16 v[0:15], v[116:119], v[120:123], v[0:15]
	v_cvt_pk_f16_f32 v33, v32, v33
	v_cvt_pk_f16_f32 v32, v36, v37
	ds_read_b128 v[36:39], v71 offset:2048
	ds_read_b128 v[116:119], v71 offset:3072
	s_nop 0
	s_nop 0
	v_min_f32 v55, 0x42fc0000, v44
	v_min_f32 v115, 0x42fc0000, v45
	s_waitcnt lgkmcnt(1)
	v_mfma_f32_32x32x16_f16 v[16:31], v[32:35], v[36:39], v[16:31]
	ds_read_b128 v[36:39], v71 offset:6144
	v_exp_f32_e32 v44, v40
	v_exp_f32_e32 v45, v41
	v_min_f32 v52, 0x42fc0000, v42
	v_min_f32 v54, 0x42fc0000, v43
	ds_read_b128 v[40:43], v71 offset:7168
	s_nop 0
	s_waitcnt lgkmcnt(1)
	v_mfma_f32_32x32x16_f16 v[0:15], v[32:35], v[36:39], v[0:15]
	v_add_f32_e64 v34, v44, 1.0
	v_add_f32_e64 v35, v45, 1.0
	s_nop 0
	v_exp_f32_e32 v32, v55
	v_exp_f32_e32 v33, v115
	v_log_f32_e32 v36, v34
	v_log_f32_e32 v37, v35
	v_exp_f32_e32 v34, v46
	v_exp_f32_e32 v35, v47
	v_exp_f32_e32 v38, v52
	v_exp_f32_e32 v39, v54
	v_pk_add_f32 v[32:33], v[32:33], 1.0 op_sel_hi:[1,0]
	v_pk_add_f32 v[34:35], v[34:35], 1.0 op_sel_hi:[1,0]
	v_log_f32_e32 v32, v32
	v_log_f32_e32 v33, v33
	v_log_f32_e32 v34, v34
	v_log_f32_e32 v35, v35
	v_pk_add_f32 v[38:39], v[38:39], 1.0 op_sel_hi:[1,0]
	v_pk_mul_f32 v[32:33], v[48:49], v[32:33] op_sel:[1,0]
	v_log_f32_e32 v38, v38
	v_log_f32_e32 v39, v39
	v_pk_mul_f32 v[34:35], v[48:49], v[34:35] op_sel:[1,0]
	v_pk_mul_f32 v[36:37], v[48:49], v[36:37] op_sel:[1,0]
	v_cvt_pk_f16_f32 v35, v34, v35
	v_cvt_pk_f16_f32 v34, v32, v33
	v_pk_mul_f32 v[32:33], v[48:49], v[38:39] op_sel:[1,0]
	v_mov_b32_e32 v54, v53
	v_cvt_pk_f16_f32 v33, v32, v33
	v_cvt_pk_f16_f32 v32, v36, v37
	v_cvt_f16_f32_e32 v36, v49
	v_mov_b32_e32 v55, v53
	v_mfma_f32_32x32x16_f16 v[16:31], v[32:35], v[116:119], v[16:31]
	v_cmp_ne_u32_sdwa s[20:21], v95, v50 src0_sel:DWORD src1_sel:WORD_1
	v_cmp_ne_u32_sdwa s[18:19], v99, v50 src0_sel:WORD_1 src1_sel:WORD_1
	s_bitcmp1_b32 s20, 0
	v_cmp_lt_i32_e64 s[2:3], s13, v64
	s_cselect_b64 s[20:21], -1, 0
	s_bitcmp0_b32 s18, 0
	s_waitcnt lgkmcnt(0)
	v_mfma_f32_32x32x16_f16 v[0:15], v[32:35], v[40:43], v[0:15]
	v_cndmask_b32_e64 v32, 0, v36, s[0:1]
	v_pack_b32_f16 v52, v32, 0
	ds_read_b128 v[32:35], v72
	ds_read_b128 v[36:39], v72 offset:1024
	s_waitcnt vmcnt(0)
	s_waitcnt vmcnt(0)
	s_waitcnt lgkmcnt(1)
	v_mfma_f32_32x32x16_f16 v[16:31], v[52:55], v[32:35], v[16:31]
	v_mov_b32_e32 v32, 0
	v_mov_b32_e32 v33, 0
	s_waitcnt lgkmcnt(0)
	v_mfma_f32_32x32x16_f16 v[0:15], v[52:55], v[36:39], v[0:15]
	s_nop 11
	v_permlane32_swap_b32_e32 v16, v0
	v_permlane32_swap_b32_e32 v17, v1
	v_permlane32_swap_b32_e32 v18, v2
	v_permlane32_swap_b32_e32 v19, v3
	v_permlane32_swap_b32_e32 v20, v4
	v_permlane32_swap_b32_e32 v21, v5
	v_permlane32_swap_b32_e32 v22, v6
	v_permlane32_swap_b32_e32 v23, v7
	v_permlane32_swap_b32_e32 v24, v8
	v_permlane32_swap_b32_e32 v25, v9
	v_permlane32_swap_b32_e32 v26, v10
	v_permlane32_swap_b32_e32 v27, v11
	v_permlane32_swap_b32_e32 v28, v12
	v_permlane32_swap_b32_e32 v29, v13
	v_permlane32_swap_b32_e32 v30, v14
	v_permlane32_swap_b32_e32 v31, v15
	v_fma_mix_f32 v32, v16, v112, v32 op_sel:[0,1,0] op_sel_hi:[0,1,0]
	v_fma_mix_f32 v33, v16, v112, v33 op_sel_hi:[0,1,0]
	s_cbranch_scc1 .LBB4_13
	v_readlane_b32 s10, v50, 0
	s_bfe_u32 s19, s10, 0x80008
	v_lshl_or_b32 v16, s19, 7, v73
	ds_read_u16 v16, v16
	s_bfe_u32 s10, s10, 0x100010
	s_lshl_b32 s10, s10, 8
	v_lshl_add_u64 v[34:35], v[60:61], 0, s[10:11]
	v_cndmask_b32_e64 v35, v63, v35, s[20:21]
	s_waitcnt lgkmcnt(0)
	v_fma_mix_f32 v16, v16, v33, v32 op_sel_hi:[1,0,0]
	v_cndmask_b32_e64 v34, v62, v34, s[20:21]
	s_mov_b64 s[20:21], -1
	v_mov_b32_e32 v32, 0
	v_mov_b32_e32 v33, 0
	global_store_dword v[34:35], v16, off sc1
